# baseline (speedup 1.0000x reference)
_Z13logits_kernelPKDv8_DF16bS1_PKfS3_PDv2_fS5_Pf:
	s_load_dwordx4 s[4:7], s[0:1], 0x0
	s_load_dwordx4 s[12:15], s[0:1], 0x10
	s_load_dwordx4 s[24:27], s[0:1], 0x20
	s_load_dwordx2 s[28:29], s[0:1], 0x30
	s_and_b32 s3, s2, 7
	s_lshl_b32 s3, s3, 1
	s_bfe_u32 s8, s2, 0x10003
	s_lshr_b32 s10, s2, 4
	s_or_b32 s3, s3, s8
	s_and_b32 s23, s2, 7
	v_lshrrev_b32_e32 v1, 6, v0
	v_and_b32_e32 v2, 63, v0
	s_movk_i32 s11, 0x3000
	v_add_u32_e32 v6, s23, v1
	v_lshlrev_b32_e32 v2, 4, v2
	v_and_b32_e32 v6, 3, v6
	v_and_b32_e32 v5, 31, v0
	v_mad_u32_u24 v6, v6, s11, v2
	v_lshlrev_b32_e32 v5, 2, v5
	s_mul_i32 s9, s23, 11
	s_lshr_b32 s9, s9, 5
	s_mul_i32 s9, s9, 3
	s_sub_i32 s23, s23, s9
	s_add_i32 s9, s23, 1
	s_cmp_ge_u32 s9, 3
	s_cselect_b32 s30, 0, s9
	s_add_i32 s9, s30, 1
	s_cmp_ge_u32 s9, 3
	s_cselect_b32 s31, 0, s9
	s_lshl_b32 s23, s23, 12
	s_lshl_b32 s30, s30, 12
	s_lshl_b32 s31, s31, 12
	s_lshl_b32 s9, s3, 9
	v_add_u32_e32 v2, s23, v6
	v_add_u32_e32 v3, s30, v6
	v_add_u32_e32 v4, s31, v6
	v_add_u32_e32 v5, s9, v5
	s_mul_i32 s8, s10, 0xc000
	s_mul_i32 s9, s3, 0x30000
	s_waitcnt lgkmcnt(0)
	s_load_dword s22, s[14:15], 0x0
	global_load_dword v248, v5, s[12:13]
	global_load_dword v249, v5, s[12:13] offset:128
	global_load_dword v250, v5, s[12:13] offset:256
	global_load_dword v251, v5, s[12:13] offset:384
	s_add_u32 s4, s4, s8
	s_addc_u32 s5, s5, 0
	s_add_u32 s6, s6, s9
	s_addc_u32 s7, s7, 0
	s_add_u32 s16, s6, 0xc000
	s_addc_u32 s17, s7, 0
	s_add_u32 s18, s6, 0x18000
	s_addc_u32 s19, s7, 0
	s_add_u32 s20, s6, 0x24000
	s_addc_u32 s21, s7, 0
	global_load_dwordx4 v[8:11], v2, s[4:5]
	global_load_dwordx4 v[56:59], v2, s[6:7]
	global_load_dwordx4 v[104:107], v2, s[16:17]
	global_load_dwordx4 v[152:155], v2, s[18:19]
	global_load_dwordx4 v[200:203], v2, s[20:21]
	global_load_dwordx4 v[12:15], v2, s[4:5] offset:1024
	global_load_dwordx4 v[60:63], v2, s[6:7] offset:1024
	global_load_dwordx4 v[108:111], v2, s[16:17] offset:1024
	global_load_dwordx4 v[156:159], v2, s[18:19] offset:1024
	global_load_dwordx4 v[204:207], v2, s[20:21] offset:1024
	global_load_dwordx4 v[16:19], v2, s[4:5] offset:2048
	global_load_dwordx4 v[64:67], v2, s[6:7] offset:2048
	global_load_dwordx4 v[112:115], v2, s[16:17] offset:2048
	global_load_dwordx4 v[160:163], v2, s[18:19] offset:2048
	global_load_dwordx4 v[208:211], v2, s[20:21] offset:2048
	global_load_dwordx4 v[20:23], v2, s[4:5] offset:3072
	global_load_dwordx4 v[68:71], v2, s[6:7] offset:3072
	global_load_dwordx4 v[116:119], v2, s[16:17] offset:3072
	global_load_dwordx4 v[164:167], v2, s[18:19] offset:3072
	global_load_dwordx4 v[212:215], v2, s[20:21] offset:3072
	global_load_dwordx4 v[24:27], v3, s[4:5]
	global_load_dwordx4 v[72:75], v3, s[6:7]
	global_load_dwordx4 v[120:123], v3, s[16:17]
	global_load_dwordx4 v[168:171], v3, s[18:19]
	global_load_dwordx4 v[216:219], v3, s[20:21]
	global_load_dwordx4 v[28:31], v3, s[4:5] offset:1024
	global_load_dwordx4 v[76:79], v3, s[6:7] offset:1024
	global_load_dwordx4 v[124:127], v3, s[16:17] offset:1024
	global_load_dwordx4 v[172:175], v3, s[18:19] offset:1024
	global_load_dwordx4 v[220:223], v3, s[20:21] offset:1024
	global_load_dwordx4 v[32:35], v3, s[4:5] offset:2048
	global_load_dwordx4 v[80:83], v3, s[6:7] offset:2048
	global_load_dwordx4 v[128:131], v3, s[16:17] offset:2048
	global_load_dwordx4 v[176:179], v3, s[18:19] offset:2048
	global_load_dwordx4 v[224:227], v3, s[20:21] offset:2048
	global_load_dwordx4 v[36:39], v3, s[4:5] offset:3072
	global_load_dwordx4 v[84:87], v3, s[6:7] offset:3072
	global_load_dwordx4 v[132:135], v3, s[16:17] offset:3072
	global_load_dwordx4 v[180:183], v3, s[18:19] offset:3072
	global_load_dwordx4 v[228:231], v3, s[20:21] offset:3072
	global_load_dwordx4 v[40:43], v4, s[4:5]
	global_load_dwordx4 v[88:91], v4, s[6:7]
	global_load_dwordx4 v[136:139], v4, s[16:17]
	global_load_dwordx4 v[184:187], v4, s[18:19]
	global_load_dwordx4 v[232:235], v4, s[20:21]
	global_load_dwordx4 v[44:47], v4, s[4:5] offset:1024
	global_load_dwordx4 v[92:95], v4, s[6:7] offset:1024
	global_load_dwordx4 v[140:143], v4, s[16:17] offset:1024
	global_load_dwordx4 v[188:191], v4, s[18:19] offset:1024
	global_load_dwordx4 v[236:239], v4, s[20:21] offset:1024
	global_load_dwordx4 v[48:51], v4, s[4:5] offset:2048
	global_load_dwordx4 v[96:99], v4, s[6:7] offset:2048
	global_load_dwordx4 v[144:147], v4, s[16:17] offset:2048
	global_load_dwordx4 v[192:195], v4, s[18:19] offset:2048
	global_load_dwordx4 v[240:243], v4, s[20:21] offset:2048
	global_load_dwordx4 v[52:55], v4, s[4:5] offset:3072
	global_load_dwordx4 v[100:103], v4, s[6:7] offset:3072
	global_load_dwordx4 v[148:151], v4, s[16:17] offset:3072
	global_load_dwordx4 v[196:199], v4, s[18:19] offset:3072
	global_load_dwordx4 v[244:247], v4, s[20:21] offset:3072
	s_waitcnt vmcnt(58)
	v_mfma_f32_32x32x16_bf16 a[0:15], v[8:11], v[56:59], 0
	s_waitcnt vmcnt(57)
	v_mfma_f32_32x32x16_bf16 a[0:15], v[8:11], v[104:107], a[0:15]
	s_waitcnt vmcnt(56)
	v_mfma_f32_32x32x16_bf16 a[0:15], v[8:11], v[152:155], a[0:15]
	s_waitcnt vmcnt(55)
	v_mfma_f32_32x32x16_bf16 a[0:15], v[8:11], v[200:203], a[0:15]
	s_waitcnt vmcnt(53)
	v_mfma_f32_32x32x16_bf16 a[0:15], v[12:15], v[60:63], a[0:15]
	s_waitcnt vmcnt(52)
	v_mfma_f32_32x32x16_bf16 a[0:15], v[12:15], v[108:111], a[0:15]
	s_waitcnt vmcnt(51)
	v_mfma_f32_32x32x16_bf16 a[0:15], v[12:15], v[156:159], a[0:15]
	s_waitcnt vmcnt(50)
	v_mfma_f32_32x32x16_bf16 a[0:15], v[12:15], v[204:207], a[0:15]
	s_waitcnt vmcnt(48)
	v_mfma_f32_32x32x16_bf16 a[0:15], v[16:19], v[64:67], a[0:15]
	s_waitcnt vmcnt(47)
	v_mfma_f32_32x32x16_bf16 a[0:15], v[16:19], v[112:115], a[0:15]
	s_waitcnt vmcnt(46)
	v_mfma_f32_32x32x16_bf16 a[0:15], v[16:19], v[160:163], a[0:15]
	s_waitcnt vmcnt(45)
	v_mfma_f32_32x32x16_bf16 a[0:15], v[16:19], v[208:211], a[0:15]
	s_waitcnt vmcnt(43)
	v_mfma_f32_32x32x16_bf16 a[0:15], v[20:23], v[68:71], a[0:15]
	s_waitcnt vmcnt(42)
	v_mfma_f32_32x32x16_bf16 a[0:15], v[20:23], v[116:119], a[0:15]
	s_waitcnt vmcnt(41)
	v_mfma_f32_32x32x16_bf16 a[0:15], v[20:23], v[164:167], a[0:15]
	s_waitcnt vmcnt(40)
	v_mfma_f32_32x32x16_bf16 a[0:15], v[20:23], v[212:215], a[0:15]
	s_waitcnt vmcnt(38)
	v_mfma_f32_32x32x16_bf16 a[0:15], v[24:27], v[72:75], a[0:15]
	s_waitcnt vmcnt(37)
	v_mfma_f32_32x32x16_bf16 a[0:15], v[24:27], v[120:123], a[0:15]
	s_waitcnt vmcnt(36)
	v_mfma_f32_32x32x16_bf16 a[0:15], v[24:27], v[168:171], a[0:15]
	s_waitcnt vmcnt(35)
	v_mfma_f32_32x32x16_bf16 a[0:15], v[24:27], v[216:219], a[0:15]
	s_waitcnt vmcnt(33)
	v_mfma_f32_32x32x16_bf16 a[0:15], v[28:31], v[76:79], a[0:15]
	s_waitcnt vmcnt(32)
	v_mfma_f32_32x32x16_bf16 a[0:15], v[28:31], v[124:127], a[0:15]
	s_waitcnt vmcnt(31)
	v_mfma_f32_32x32x16_bf16 a[0:15], v[28:31], v[172:175], a[0:15]
	s_waitcnt vmcnt(30)
	v_mfma_f32_32x32x16_bf16 a[0:15], v[28:31], v[220:223], a[0:15]
	s_waitcnt vmcnt(28)
	v_mfma_f32_32x32x16_bf16 a[0:15], v[32:35], v[80:83], a[0:15]
	s_waitcnt vmcnt(27)
	v_mfma_f32_32x32x16_bf16 a[0:15], v[32:35], v[128:131], a[0:15]
	s_waitcnt vmcnt(26)
	v_mfma_f32_32x32x16_bf16 a[0:15], v[32:35], v[176:179], a[0:15]
	s_waitcnt vmcnt(25)
	v_mfma_f32_32x32x16_bf16 a[0:15], v[32:35], v[224:227], a[0:15]
	s_waitcnt vmcnt(23)
	v_mfma_f32_32x32x16_bf16 a[0:15], v[36:39], v[84:87], a[0:15]
	s_waitcnt vmcnt(22)
	v_mfma_f32_32x32x16_bf16 a[0:15], v[36:39], v[132:135], a[0:15]
	s_waitcnt vmcnt(21)
	v_mfma_f32_32x32x16_bf16 a[0:15], v[36:39], v[180:183], a[0:15]
	s_waitcnt vmcnt(20)
	v_mfma_f32_32x32x16_bf16 a[0:15], v[36:39], v[228:231], a[0:15]
	s_waitcnt vmcnt(18)
	v_mfma_f32_32x32x16_bf16 a[0:15], v[40:43], v[88:91], a[0:15]
	s_waitcnt vmcnt(17)
	v_mfma_f32_32x32x16_bf16 a[0:15], v[40:43], v[136:139], a[0:15]
	s_waitcnt vmcnt(16)
	v_mfma_f32_32x32x16_bf16 a[0:15], v[40:43], v[184:187], a[0:15]
	s_waitcnt vmcnt(15)
	v_mfma_f32_32x32x16_bf16 a[0:15], v[40:43], v[232:235], a[0:15]
	s_waitcnt vmcnt(13)
	v_mfma_f32_32x32x16_bf16 a[0:15], v[44:47], v[92:95], a[0:15]
	s_waitcnt vmcnt(12)
	v_mfma_f32_32x32x16_bf16 a[0:15], v[44:47], v[140:143], a[0:15]
	s_waitcnt vmcnt(11)
	v_mfma_f32_32x32x16_bf16 a[0:15], v[44:47], v[188:191], a[0:15]
	s_waitcnt vmcnt(10)
	v_mfma_f32_32x32x16_bf16 a[0:15], v[44:47], v[236:239], a[0:15]
	v_add_f32_e32 v8, 0, v248
	v_add_f32_e32 v8, v8, v249
	v_add_f32_e32 v8, v8, v250
	v_add_f32_e32 v8, v8, v251
	v_mov_b32_e32 v9, 0x3fb8aa3b
	s_waitcnt lgkmcnt(0)
	v_mul_f32_e32 v9, s22, v9
	v_exp_f32_e32 v9, v9
	v_add_f32_e32 v10, 0x2b8cbccc, v8
	v_div_scale_f32 v11, s[8:9], v10, v10, v9
	v_rcp_f32_e32 v12, v11
	v_div_scale_f32 v13, vcc, v9, v10, v9
	v_fma_f32 v14, -v11, v12, 1.0
	v_fmac_f32_e32 v12, v14, v12
	v_mul_f32_e32 v14, v13, v12
	v_fma_f32 v15, -v11, v14, v13
	v_fmac_f32_e32 v14, v15, v12
	v_fma_f32 v11, -v11, v14, v13
	v_div_fmas_f32 v11, v11, v12, v14
	v_div_fixup_f32 v9, v11, v10, v9
	v_lshlrev_b32_e32 v10, 2, v0
	v_add_u32_e32 v10, 0x4000, v10
	v_cmp_gt_u32_e32 vcc, 32, v0
	s_and_saveexec_b64 s[8:9], vcc
	ds_write2_b32 v10, v8, v9 offset0:128 offset1:160
	s_mov_b64 exec, s[8:9]
	s_waitcnt vmcnt(8)
	v_mfma_f32_32x32x16_bf16 a[0:15], v[48:51], v[96:99], a[0:15]
	s_waitcnt vmcnt(7)
	v_mfma_f32_32x32x16_bf16 a[0:15], v[48:51], v[144:147], a[0:15]
	s_waitcnt vmcnt(6)
	v_mfma_f32_32x32x16_bf16 a[0:15], v[48:51], v[192:195], a[0:15]
	s_waitcnt vmcnt(5)
	v_mfma_f32_32x32x16_bf16 a[0:15], v[48:51], v[240:243], a[0:15]
	v_mul_u32_u24_e32 v1, 0x1080, v1
	s_movk_i32 s4, 0x7f
	s_movk_i32 s6, 0x84
	v_cmp_lt_u32_e32 vcc, s4, v0
	v_lshrrev_b32_e32 v11, 3, v0
	v_and_b32_e32 v10, 31, v0
	v_and_b32_e32 v11, 4, v11
	v_mul_u32_u24_e32 v11, 0x84, v11
	v_lshlrev_b32_e32 v9, 2, v10
	v_bfe_u32 v6, v0, 2, 5
	v_and_b32_e32 v7, 3, v0
	v_add3_u32 v1, v1, v11, v9
	v_lshlrev_b32_e32 v8, 3, v7
	s_waitcnt vmcnt(3)
	v_mfma_f32_32x32x16_bf16 a[0:15], v[52:55], v[100:103], a[0:15]
	s_waitcnt vmcnt(2)
	v_mfma_f32_32x32x16_bf16 a[0:15], v[52:55], v[148:151], a[0:15]
	s_waitcnt vmcnt(1)
	v_mfma_f32_32x32x16_bf16 a[0:15], v[52:55], v[196:199], a[0:15]
	s_waitcnt vmcnt(0)
	v_mfma_f32_32x32x16_bf16 a[0:15], v[52:55], v[244:247], a[0:15]
	s_nop 11
	ds_write_b32 v1, a0
	ds_write_b32 v1, a1 offset:132
	ds_write_b32 v1, a2 offset:264
	ds_write_b32 v1, a3 offset:396
	ds_write_b32 v1, a4 offset:1056
	ds_write_b32 v1, a5 offset:1188
	ds_write_b32 v1, a6 offset:1320
	ds_write_b32 v1, a7 offset:1452
	ds_write_b32 v1, a8 offset:2112
	ds_write_b32 v1, a9 offset:2244
	ds_write_b32 v1, a10 offset:2376
	ds_write_b32 v1, a11 offset:2508
	ds_write_b32 v1, a12 offset:3168
	ds_write_b32 v1, a13 offset:3300
	ds_write_b32 v1, a14 offset:3432
	ds_write_b32 v1, a15 offset:3564
	v_bfe_u32 v6, v0, 2, 5
	v_and_b32_e32 v7, 3, v0
	v_lshlrev_b32_e32 v9, 3, v7
	v_readfirstlane_b32 s30, v0
	v_sub_u32_e32 v10, v6, v9
	s_waitcnt lgkmcnt(0)
	s_barrier
	s_cmpk_ge_u32 s30, 0x80
	s_cbranch_scc1 .Llg_k1
	v_mul_u32_u24_e32 v2, 0x84, v6
	v_lshlrev_b32_e32 v8, 5, v7
	v_add_u32_e32 v2, v2, v8
	v_add_u32_e32 v8, 0x4280, v8
	v_add_u32_e32 v3, 0x1080, v2
	v_add_u32_e32 v4, 0x2100, v2
	v_add_u32_e32 v5, 0x3180, v2
	ds_read_b128 v[48:51], v8
	ds_read_b128 v[52:55], v8 offset:16
	ds_read2_b32 v[16:17], v2 offset0:0 offset1:1
	ds_read2_b32 v[18:19], v2 offset0:2 offset1:3
	ds_read2_b32 v[20:21], v2 offset0:4 offset1:5
	ds_read2_b32 v[22:23], v2 offset0:6 offset1:7
	ds_read2_b32 v[24:25], v3 offset0:0 offset1:1
	ds_read2_b32 v[26:27], v3 offset0:2 offset1:3
	ds_read2_b32 v[28:29], v3 offset0:4 offset1:5
	ds_read2_b32 v[30:31], v3 offset0:6 offset1:7
	ds_read2_b32 v[32:33], v4 offset0:0 offset1:1
	ds_read2_b32 v[34:35], v4 offset0:2 offset1:3
	ds_read2_b32 v[36:37], v4 offset0:4 offset1:5
	ds_read2_b32 v[38:39], v4 offset0:6 offset1:7
	s_waitcnt lgkmcnt(4)
	ds_read2_b32 v[40:41], v5 offset0:0 offset1:1
	ds_read2_b32 v[42:43], v5 offset0:2 offset1:3
	ds_read2_b32 v[44:45], v5 offset0:4 offset1:5
	ds_read2_b32 v[46:47], v5 offset0:6 offset1:7
	s_waitcnt lgkmcnt(0)
	s_branch .Llg_join
